# x0a: x0_row loop issues its four row loads together and defers the bf16 stores (one round trip per row instead of four)
# baseline (speedup 1.0000x reference)
; __device__ __forceinline__ float wave_sum(float v) { return half_sum(sum32(v)); }
; __device__ __forceinline__ void st_bf4(bf16_t* p, f32x4 v) { u32x2 w; w.x = cvt_pk_bf16(v[0], v[1]); w.y = cvt_pk_bf16(v[2], v[3]); *(u32x2*)p = w; }
; __device__ __forceinline__ void x0_row(const float* xrow, bf16_t* xbrow, float* prow, int lane) {
;     const f32x4* xr = (const f32x4*)xrow + lane; float s = 0.f;
; #pragma unroll
;     for (int j = 0; j < 4; ++j) { const f32x4 v = xr[64 * j]; s += (v[0] * v[0] + v[1] * v[1]) + (v[2] * v[2] + v[3] * v[3]); st_bf4(xbrow + j * 256 + lane * 4, v); }
;     s = wave_sum(s);
;     if (lane < 16) prow[lane] = lane == 0 ? s : 0.f;
; }
.LBB0_433:
	v_lshl_add_u64 v[10:11], s[52:53], 0, v[4:5]
	global_load_dwordx4 v[6:9], v[0:1], off offset:-2048
	v_add_co_u32_e64 v22, s[6:7], s3, v10
	s_nop 1
	v_addc_co_u32_e64 v23, s[6:7], 0, v11, s[6:7]
	global_load_dwordx4 v[10:13], v[0:1], off offset:-1024
	global_load_dwordx4 v[14:17], v[0:1], off
	global_load_dwordx4 v[18:21], v[0:1], off offset:1024
	s_waitcnt vmcnt(3)
	v_cvt_pk_bf16_f32 v24, v6, v7
	v_cvt_pk_bf16_f32 v25, v8, v9
	s_waitcnt vmcnt(2)
	v_cvt_pk_bf16_f32 v26, v10, v11
	v_cvt_pk_bf16_f32 v27, v12, v13
	s_waitcnt vmcnt(1)
	v_cvt_pk_bf16_f32 v28, v14, v15
	v_cvt_pk_bf16_f32 v29, v16, v17
	v_mul_f32_e32 v7, v7, v7
	v_mul_f32_e32 v9, v9, v9
	v_fmac_f32_e32 v7, v6, v6
	v_fmac_f32_e32 v9, v8, v8
	v_add_f32_e32 v6, v7, v9
	v_mul_f32_e32 v7, v11, v11
	v_mul_f32_e32 v8, v13, v13
	v_fmac_f32_e32 v7, v10, v10
	v_fmac_f32_e32 v8, v12, v12
	v_add_f32_e32 v7, v7, v8
	v_add_f32_e32 v6, v6, v7
	v_mul_f32_e32 v7, v15, v15
	v_mul_f32_e32 v8, v17, v17
	v_fmac_f32_e32 v7, v14, v14
	v_fmac_f32_e32 v8, v16, v16
	v_add_f32_e32 v7, v7, v8
	v_add_f32_e32 v6, v6, v7
	s_waitcnt vmcnt(0)
	v_mul_f32_e32 v7, v19, v19
	v_mul_f32_e32 v8, v21, v21
	v_fmac_f32_e32 v7, v18, v18
	v_fmac_f32_e32 v8, v20, v20
	v_add_f32_e32 v7, v7, v8
	v_add_f32_e32 v6, v6, v7
	s_waitcnt lgkmcnt(0)
	s_nop 1
	v_add_f32_dpp v6, v6, v6 quad_perm:[1,0,3,2] row_mask:0xf bank_mask:0xf
	s_waitcnt lgkmcnt(0)
	s_nop 1
	v_add_f32_dpp v6, v6, v6 quad_perm:[2,3,0,1] row_mask:0xf bank_mask:0xf
	s_waitcnt lgkmcnt(0)
	s_nop 1
	v_add_f32_dpp v6, v6, v6 row_half_mirror row_mask:0xf bank_mask:0xf
	s_waitcnt lgkmcnt(0)
	s_nop 1
	v_add_f32_dpp v8, v6, v6 row_mirror row_mask:0xf bank_mask:0xf
	ds_swizzle_b32 v9, v8 offset:swizzle(SWAP,16)
	v_cvt_pk_bf16_f32 v6, v18, v19
	v_cvt_pk_bf16_f32 v7, v20, v21
	global_store_dwordx2 v[22:23], v[24:25], off
	global_store_dwordx2 v[22:23], v[26:27], off offset:512
	global_store_dwordx2 v[22:23], v[28:29], off offset:1024
	global_store_dwordx2 v[22:23], v[6:7], off offset:1536
	s_waitcnt lgkmcnt(0)
	v_add_f32_e32 v6, v8, v9
	v_mov_b32_e32 v7, v6
	s_nop 1
	v_permlane32_swap_b32_e32 v6, v7
	s_and_saveexec_b64 s[6:7], vcc
	s_cbranch_execz .LBB0_432
	v_add_f32_e32 v6, v6, v7
	v_cndmask_b32_e64 v8, 0, v6, s[4:5]
	v_lshl_add_u64 v[6:7], s[52:53], 0, v[2:3]
	global_store_dword v[6:7], v8, off
	s_branch .LBB0_432
